# v12 plus 4x-pipelined x->bf16/e4m3 conversion loop in the prologue phase (the previous measurement with this text was taken on a different diagnostic file by mistake)
# baseline (speedup 1.0000x reference)
; DI unsigned cvt_pk_bf16(float lo, float hi) { const f32x2_t v = {lo, hi}; return __builtin_bit_cast(unsigned, __builtin_convertvector(v, bf16x2_t)); }
; DI unsigned pk4_fp8(float a, float b, float c, float d) { int w = __builtin_amdgcn_cvt_pk_fp8_f32(sat8(a), sat8(b), 0, false); w = __builtin_amdgcn_cvt_pk_fp8_f32(sat8(c), sat8(d), w, true); return (unsigned)w; }
; DI KArgP kargs() { KArgP p = (KArgP)__builtin_amdgcn_kernarg_segment_ptr(); asm volatile("" : "+s"(p)); return p; }
; __global__ void __launch_bounds__(512, 2) mk_fwd(FArgs args) {
;     ...
;         { const size_t n4 = (size_t)NTOK * D_ / 4; const f32x4* s = (const f32x4*)kargs()->in[0]; u32x2* d = (u32x2*)XB;
;           unsigned* d8 = (unsigned*)(ws + WS_XB8);
;           for (size_t i = (size_t)bid * 512 + tid; i < n4; i += (size_t)G * 512) { const f32x4 v = s[i]; d[i] = (u32x2){pg8::cvt_pk_bf16(v.x, v.y), pg8::cvt_pk_bf16(v.z, v.w)}; d8[i] = pg8::pk4_fp8(v.x * X_SC, v.y * X_SC, v.z * X_SC, v.w * X_SC); } }
.LBB0_126:
	s_ashr_i32 s3, s2, 31
	s_lshl_b64 s[8:9], s[2:3], 9
	v_ashrrev_i32_e32 v129, 31, v128
	s_waitcnt vmcnt(23)
	v_lshl_add_u64 v[0:1], s[8:9], 0, v[128:129]
	s_mov_b64 s[8:9], 0x400000
	s_mov_b64 s[10:11], s[0:1]
	v_cmp_gt_u64_e32 vcc, s[8:9], v[0:1]
	s_and_saveexec_b64 s[8:9], vcc
	s_cbranch_execz .LBB0_129
	s_ashr_i32 s35, s34, 31
	s_load_dwordx2 s[16:17], s[10:11], 0x0
	s_lshl_b64 s[10:11], s[34:35], 9
	s_lshl_b64 s[12:13], s[2:3], 11
	s_add_u32 s12, s4, s12
	s_addc_u32 s13, s5, s13
	v_lshl_add_u64 v[2:3], v[128:129], 2, s[12:13]
	s_mov_b64 s[12:13], 0x6a300000
	v_lshl_add_u64 v[2:3], v[2:3], 0, s[12:13]
	s_lshl_b64 s[12:13], s[34:35], 11
	s_lshl_b64 s[14:15], s[2:3], 12
	s_add_u32 s14, s4, s14
	s_addc_u32 s15, s5, s15
	s_waitcnt vmcnt(22)
	v_lshl_add_u64 v[4:5], v[128:129], 3, s[14:15]
	s_mov_b64 s[14:15], 0x200000
	v_lshl_add_u64 v[4:5], v[4:5], 0, s[14:15]
	s_lshl_b64 s[14:15], s[34:35], 12
	s_lshl_b64 s[18:19], s[2:3], 13
	s_waitcnt lgkmcnt(0)
	s_add_u32 s16, s16, s18
	s_addc_u32 s17, s17, s19
	v_lshl_add_u64 v[6:7], v[128:129], 4, s[16:17]
	s_lshl_b64 s[16:17], s[34:35], 13
	s_mov_b64 s[18:19], 0
	s_mov_b32 s22, 0xc3e00000
	s_waitcnt vmcnt(21)
	v_mov_b32_e32 v10, 0x43e00000
	s_mov_b64 s[20:21], 0x3fffff
	v_mov_b64_e32 v[8:9], v[0:1]
	s_waitcnt vmcnt(0)
	s_mul_i32 s24, s10, 3
	s_mov_b32 s25, 0
.Lmy_x4:
	v_lshl_add_u64 v[58:59], v[8:9], 0, s[24:25]
	v_cmp_ge_u64_e32 vcc, s[20:21], v[58:59]
	s_cmp_eq_u64 vcc, exec
	s_cbranch_scc0 .Lmy_x4_exit
	v_lshl_add_u64 v[36:37], v[6:7], 0, s[16:17]
	v_lshl_add_u64 v[38:39], v[36:37], 0, s[16:17]
	v_lshl_add_u64 v[40:41], v[38:39], 0, s[16:17]
	global_load_dwordx4 v[20:23], v[6:7], off
	global_load_dwordx4 v[24:27], v[36:37], off
	global_load_dwordx4 v[28:31], v[38:39], off
	global_load_dwordx4 v[32:35], v[40:41], off
	v_lshl_add_u64 v[6:7], v[40:41], 0, s[16:17]
	v_lshl_add_u64 v[8:9], v[58:59], 0, s[10:11]
	s_waitcnt vmcnt(3)
	v_mov_b32_e32 v44, 0
	v_cvt_pk_bf16_f32 v42, v20, v21
	v_mul_f32_e32 v18, 0x41800000, v20
	v_mul_f32_e32 v19, 0x41800000, v21
	v_med3_f32 v18, v18, s22, v10
	v_med3_f32 v19, v19, s22, v10
	v_cvt_pk_fp8_f32 v44, v18, v19
	v_cvt_pk_bf16_f32 v43, v22, v23
	v_mul_f32_e32 v18, 0x41800000, v22
	v_mul_f32_e32 v19, 0x41800000, v23
	v_med3_f32 v18, v18, s22, v10
	v_med3_f32 v19, v19, s22, v10
	v_cvt_pk_fp8_f32 v44, v18, v19 op_sel:[0,0,1]
	global_store_dwordx2 v[4:5], v[42:43], off
	v_lshl_add_u64 v[4:5], v[4:5], 0, s[14:15]
	global_store_dword v[2:3], v44, off
	v_lshl_add_u64 v[2:3], v[2:3], 0, s[12:13]
	s_waitcnt vmcnt(4)
	v_mov_b32_e32 v48, 0
	v_cvt_pk_bf16_f32 v46, v24, v25
	v_mul_f32_e32 v18, 0x41800000, v24
	v_mul_f32_e32 v19, 0x41800000, v25
	v_med3_f32 v18, v18, s22, v10
	v_med3_f32 v19, v19, s22, v10
	v_cvt_pk_fp8_f32 v48, v18, v19
	v_cvt_pk_bf16_f32 v47, v26, v27
	v_mul_f32_e32 v18, 0x41800000, v26
	v_mul_f32_e32 v19, 0x41800000, v27
	v_med3_f32 v18, v18, s22, v10
	v_med3_f32 v19, v19, s22, v10
	v_cvt_pk_fp8_f32 v48, v18, v19 op_sel:[0,0,1]
	global_store_dwordx2 v[4:5], v[46:47], off
	v_lshl_add_u64 v[4:5], v[4:5], 0, s[14:15]
	global_store_dword v[2:3], v48, off
	v_lshl_add_u64 v[2:3], v[2:3], 0, s[12:13]
	s_waitcnt vmcnt(5)
	v_mov_b32_e32 v52, 0
	v_cvt_pk_bf16_f32 v50, v28, v29
	v_mul_f32_e32 v18, 0x41800000, v28
	v_mul_f32_e32 v19, 0x41800000, v29
	v_med3_f32 v18, v18, s22, v10
	v_med3_f32 v19, v19, s22, v10
	v_cvt_pk_fp8_f32 v52, v18, v19
	v_cvt_pk_bf16_f32 v51, v30, v31
	v_mul_f32_e32 v18, 0x41800000, v30
	v_mul_f32_e32 v19, 0x41800000, v31
	v_med3_f32 v18, v18, s22, v10
	v_med3_f32 v19, v19, s22, v10
	v_cvt_pk_fp8_f32 v52, v18, v19 op_sel:[0,0,1]
	global_store_dwordx2 v[4:5], v[50:51], off
	v_lshl_add_u64 v[4:5], v[4:5], 0, s[14:15]
	global_store_dword v[2:3], v52, off
	v_lshl_add_u64 v[2:3], v[2:3], 0, s[12:13]
	s_waitcnt vmcnt(6)
	v_mov_b32_e32 v56, 0
	v_cvt_pk_bf16_f32 v54, v32, v33
	v_mul_f32_e32 v18, 0x41800000, v32
	v_mul_f32_e32 v19, 0x41800000, v33
	v_med3_f32 v18, v18, s22, v10
	v_med3_f32 v19, v19, s22, v10
	v_cvt_pk_fp8_f32 v56, v18, v19
	v_cvt_pk_bf16_f32 v55, v34, v35
	v_mul_f32_e32 v18, 0x41800000, v34
	v_mul_f32_e32 v19, 0x41800000, v35
	v_med3_f32 v18, v18, s22, v10
	v_med3_f32 v19, v19, s22, v10
	v_cvt_pk_fp8_f32 v56, v18, v19 op_sel:[0,0,1]
	global_store_dwordx2 v[4:5], v[54:55], off
	v_lshl_add_u64 v[4:5], v[4:5], 0, s[14:15]
	global_store_dword v[2:3], v56, off
	v_lshl_add_u64 v[2:3], v[2:3], 0, s[12:13]
	s_branch .Lmy_x4
.Lmy_x4_exit:
	v_cmp_ge_u64_e32 vcc, s[20:21], v[8:9]
	s_and_b64 exec, exec, vcc
	s_cbranch_execz .LBB0_129
